# v18
# baseline (speedup 1.0000x reference)
.LBB2_31:
	s_add_i32 s17, s17, 3
	s_ashr_i32 s2, s17, 2
	v_subrev_u32_e32 v8, s6, v8
	s_max_i32 s6, s2, 1
	s_setprio 0
	s_add_i32 s2, s4, s7
	s_add_i32 s2, s2, s16
	s_add_i32 s2, s2, s6
	s_mul_hi_u32 s22, s2, 0xaaaaaaab
	s_lshr_b32 s22, s22, 1
	v_mov_b32_e32 v45, 0
	s_mov_b32 s2, 0x3a800000
	s_mov_b32 s17, 0
	s_mov_b32 s23, 0xc040c00
	s_mov_b32 s24, 0xc050c01
	s_mov_b32 s25, 0xc060c02
	s_mov_b32 s26, 0xc070c03
	s_mov_b32 s3, 0xc3000000
	v_mov_b32_e32 v9, 0x186a0
	s_mov_b32 s5, 0
	v_mov_b32_e32 v60, 0
	v_mov_b32_e32 v42, v45
	v_mov_b32_e32 v43, v45
	v_mov_b32_e32 v36, v45
	v_mov_b32_e32 v37, v45
	v_mov_b32_e32 v30, v45
	v_mov_b32_e32 v31, v45
	v_mov_b32_e32 v53, 0
	s_lshl_b32 s28, s27, 2
	v_add_u32_e32 v79, s28, v3
	v_lshl_add_u32 v79, v79, 2, v2
	ds_read_b32 v80, v79 offset:15360
	ds_read_b32 v81, v79 offset:15364
	ds_read_b32 v82, v79 offset:15368
	ds_read_b32 v79, v79 offset:15372
	v_cmp_lt_i32_e32 vcc, s28, v5
	s_or_b32 s29, s28, 1
	s_or_b32 s30, s28, 2
	s_waitcnt lgkmcnt(0)
	v_cndmask_b32_e32 v87, v9, v80, vcc
	v_cmp_lt_i32_e32 vcc, s29, v5
	s_or_b32 s31, s28, 3
	s_nop 0
	v_cndmask_b32_e32 v88, v9, v81, vcc
	v_cmp_lt_i32_e32 vcc, s30, v5
	v_lshl_or_b32 v83, v87, 7, v66
	v_lshlrev_b32_e32 v87, 2, v87
	v_cndmask_b32_e32 v89, v9, v82, vcc
	v_cmp_lt_i32_e32 vcc, s31, v5
	v_lshl_or_b32 v84, v88, 7, v66
	v_lshl_or_b32 v85, v89, 7, v66
	v_cndmask_b32_e32 v90, v9, v79, vcc
	v_lshl_or_b32 v86, v90, 7, v66
	v_lshlrev_b32_e32 v88, 2, v88
	v_lshlrev_b32_e32 v89, 2, v89
	v_lshlrev_b32_e32 v90, 2, v90
	s_add_i32 s27, s27, 1
	global_load_dwordx2 v[46:47], v83, s[10:11]
	global_load_dwordx2 v[48:49], v84, s[10:11]
	global_load_dwordx2 v[92:93], v85, s[10:11]
	global_load_dwordx2 v[94:95], v86, s[10:11]
	global_load_dword v63, v87, s[12:13]
	global_load_dword v64, v88, s[12:13]
	global_load_dword v65, v89, s[12:13]
	global_load_dword v91, v90, s[12:13]
	s_cmp_lg_u32 s27, s21
	s_cbranch_scc1 .Lp2_34
	s_cmp_eq_u32 s20, 0
	s_cbranch_scc1 .Lp2_32
	s_add_i32 s27, s20, 1
	s_mov_b32 s20, 2
	s_cmp_eq_u32 s27, 2
	v_mov_b32_e32 v3, v7
	v_mov_b32_e32 v5, v51
	s_mov_b32 s21, s16
	s_cbranch_scc1 .Lp2_33
	s_cmp_eq_u32 s27, 3
	s_cselect_b64 vcc, -1, 0
	s_and_b64 s[20:21], vcc, exec
	v_cndmask_b32_e32 v5, 0, v52, vcc
	s_cselect_b32 s21, s6, 0x7fffffff
	s_mov_b32 s20, s27
	v_mov_b32_e32 v3, v8
	s_branch .Lp2_33

.Lp2_34:
	s_branch .LBB2_35

.LBB2_35:
	s_lshl_b32 s28, s27, 2
	v_add_u32_e32 v79, s28, v3
	v_lshl_add_u32 v79, v79, 2, v2
	ds_read_b32 v80, v79 offset:15360
	ds_read_b32 v81, v79 offset:15364
	ds_read_b32 v82, v79 offset:15368
	ds_read_b32 v79, v79 offset:15372
	v_cmp_lt_i32_e32 vcc, s28, v5
	s_or_b32 s29, s28, 1
	s_or_b32 s30, s28, 2
	s_waitcnt lgkmcnt(0)
	v_cndmask_b32_e32 v87, v9, v80, vcc
	v_cmp_lt_i32_e32 vcc, s29, v5
	s_or_b32 s31, s28, 3
	s_nop 0
	v_cndmask_b32_e32 v88, v9, v81, vcc
	v_cmp_lt_i32_e32 vcc, s30, v5
	v_lshl_or_b32 v83, v87, 7, v66
	v_lshlrev_b32_e32 v87, 2, v87
	v_cndmask_b32_e32 v89, v9, v82, vcc
	v_cmp_lt_i32_e32 vcc, s31, v5
	v_lshl_or_b32 v84, v88, 7, v66
	v_lshl_or_b32 v85, v89, 7, v66
	v_cndmask_b32_e32 v90, v9, v79, vcc
	v_lshl_or_b32 v86, v90, 7, v66
	v_lshlrev_b32_e32 v88, 2, v88
	v_lshlrev_b32_e32 v89, 2, v89
	v_lshlrev_b32_e32 v90, 2, v90
	s_waitcnt vmcnt(18)
	v_cvt_pk_f16_f32 v10, v61, v62
	v_perm_b32 v11, v40, v38, s23
	v_dot2c_f32_f16_e32 v60, v11, v10
	v_perm_b32 v11, v40, v38, s24
	v_dot2c_f32_f16_e32 v42, v11, v10
	v_perm_b32 v11, v40, v38, s25
	v_dot2c_f32_f16_e32 v43, v11, v10
	v_perm_b32 v11, v40, v38, s26
	v_dot2c_f32_f16_e32 v36, v11, v10
	v_perm_b32 v11, v41, v39, s23
	v_dot2c_f32_f16_e32 v37, v11, v10
	v_perm_b32 v11, v41, v39, s24
	v_dot2c_f32_f16_e32 v30, v11, v10
	v_perm_b32 v11, v41, v39, s25
	v_dot2c_f32_f16_e32 v31, v11, v10
	v_perm_b32 v11, v41, v39, s26
	v_dot2c_f32_f16_e32 v53, v11, v10
	v_dot2c_f32_f16_e32 v45, 0x3c003c00, v10
	s_waitcnt vmcnt(16)
	v_cvt_pk_f16_f32 v10, v58, v59
	v_perm_b32 v11, v34, v32, s23
	v_dot2c_f32_f16_e32 v60, v11, v10
	v_perm_b32 v11, v34, v32, s24
	v_dot2c_f32_f16_e32 v42, v11, v10
	v_perm_b32 v11, v34, v32, s25
	v_dot2c_f32_f16_e32 v43, v11, v10
	v_perm_b32 v11, v34, v32, s26
	v_dot2c_f32_f16_e32 v36, v11, v10
	v_perm_b32 v11, v35, v33, s23
	v_dot2c_f32_f16_e32 v37, v11, v10
	v_perm_b32 v11, v35, v33, s24
	v_dot2c_f32_f16_e32 v30, v11, v10
	v_perm_b32 v11, v35, v33, s25
	v_dot2c_f32_f16_e32 v31, v11, v10
	v_perm_b32 v11, v35, v33, s26
	s_add_i32 s5, s5, 1
	v_dot2c_f32_f16_e32 v53, v11, v10
	s_cmp_lg_u32 s5, s4
	v_dot2c_f32_f16_e32 v45, 0x3c003c00, v10
	s_cbranch_scc1 .LBB2_43
	v_cmp_gt_i32_e32 vcc, 15, v18
	s_and_saveexec_b64 s[4:5], vcc
	s_cbranch_execz .LBB2_38
	v_max_i32_e32 v10, 1, v44
	v_cvt_f32_u32_e32 v10, v10
	v_rcp_iflag_f32_e32 v44, v10
	s_nop 0
	v_pk_mul_f32 v[10:11], v[44:45], s[2:3]
	s_nop 0
	v_mul_f32_e32 v14, 0x4b800000, v10
	v_pk_mul_f32 v[16:17], v[10:11], v[10:11] op_sel:[0,1] op_sel_hi:[1,0]
	s_nop 0
	v_fma_mixlo_f16 v15, v60, v14, v16
	v_pk_fma_f32 v[10:11], v[42:43], v[14:15], v[16:17] op_sel_hi:[1,0,0]
	v_pk_fma_f32 v[12:13], v[36:37], v[14:15], v[16:17] op_sel_hi:[1,0,0]
	v_pk_fma_f32 v[30:31], v[30:31], v[14:15], v[16:17] op_sel_hi:[1,0,0]
	v_cvt_pk_f16_f32 v11, v10, v11
	v_cvt_pk_f16_f32 v12, v12, v13
	v_cvt_pk_f16_f32 v13, v30, v31
	v_pack_b32_f16 v10, v15, v11
	v_alignbit_b32 v11, v12, v11, 16
	v_alignbit_b32 v12, v13, v12, 16
	v_lshrrev_b32_e32 v13, 16, v13
	v_fma_mixhi_f16 v13, v53, v14, v16
	v_add_u32_e32 v14, v18, v77
	v_xor_b32_e32 v15, v14, v0
	v_lshlrev_b32_e32 v15, 4, v15
	v_and_b32_e32 v15, 0xf0, v15
	v_lshl_or_b32 v14, v14, 8, v15
	ds_write_b128 v14, v[10:13]

.LBB2_49:
	s_lshl_b32 s28, s27, 2
	v_add_u32_e32 v79, s28, v3
	v_lshl_add_u32 v79, v79, 2, v2
	ds_read_b32 v80, v79 offset:15360
	ds_read_b32 v81, v79 offset:15364
	ds_read_b32 v82, v79 offset:15368
	ds_read_b32 v79, v79 offset:15372
	v_cmp_lt_i32_e32 vcc, s28, v5
	s_or_b32 s29, s28, 1
	s_or_b32 s30, s28, 2
	s_waitcnt lgkmcnt(0)
	v_cndmask_b32_e32 v87, v9, v80, vcc
	v_cmp_lt_i32_e32 vcc, s29, v5
	s_or_b32 s31, s28, 3
	s_nop 0
	v_cndmask_b32_e32 v88, v9, v81, vcc
	v_cmp_lt_i32_e32 vcc, s30, v5
	v_lshl_or_b32 v83, v87, 7, v66
	v_lshlrev_b32_e32 v87, 2, v87
	v_cndmask_b32_e32 v89, v9, v82, vcc
	v_cmp_lt_i32_e32 vcc, s31, v5
	v_lshl_or_b32 v84, v88, 7, v66
	v_lshl_or_b32 v85, v89, 7, v66
	v_cndmask_b32_e32 v90, v9, v79, vcc
	v_lshl_or_b32 v86, v90, 7, v66
	v_lshlrev_b32_e32 v88, 2, v88
	v_lshlrev_b32_e32 v89, 2, v89
	v_lshlrev_b32_e32 v90, 2, v90
	s_waitcnt vmcnt(18)
	v_cvt_pk_f16_f32 v10, v56, v57
	v_perm_b32 v11, v28, v26, s23
	v_dot2c_f32_f16_e32 v60, v11, v10
	v_perm_b32 v11, v28, v26, s24
	v_dot2c_f32_f16_e32 v42, v11, v10
	v_perm_b32 v11, v28, v26, s25
	v_dot2c_f32_f16_e32 v43, v11, v10
	v_perm_b32 v11, v28, v26, s26
	v_dot2c_f32_f16_e32 v36, v11, v10
	v_perm_b32 v11, v29, v27, s23
	v_dot2c_f32_f16_e32 v37, v11, v10
	v_perm_b32 v11, v29, v27, s24
	v_dot2c_f32_f16_e32 v30, v11, v10
	v_perm_b32 v11, v29, v27, s25
	v_dot2c_f32_f16_e32 v31, v11, v10
	v_perm_b32 v11, v29, v27, s26
	v_dot2c_f32_f16_e32 v53, v11, v10
	v_dot2c_f32_f16_e32 v45, 0x3c003c00, v10
	s_waitcnt vmcnt(16)
	v_cvt_pk_f16_f32 v10, v54, v55
	v_perm_b32 v11, v24, v22, s23
	v_dot2c_f32_f16_e32 v60, v11, v10
	v_perm_b32 v11, v24, v22, s24
	v_dot2c_f32_f16_e32 v42, v11, v10
	v_perm_b32 v11, v24, v22, s25
	v_dot2c_f32_f16_e32 v43, v11, v10
	v_perm_b32 v11, v24, v22, s26
	v_dot2c_f32_f16_e32 v36, v11, v10
	v_perm_b32 v11, v25, v23, s23
	v_dot2c_f32_f16_e32 v37, v11, v10
	v_perm_b32 v11, v25, v23, s24
	v_dot2c_f32_f16_e32 v30, v11, v10
	v_perm_b32 v11, v25, v23, s25
	v_dot2c_f32_f16_e32 v31, v11, v10
	v_perm_b32 v11, v25, v23, s26
	s_add_i32 s5, s5, 1
	v_dot2c_f32_f16_e32 v53, v11, v10
	s_cmp_lg_u32 s5, s4
	v_dot2c_f32_f16_e32 v45, 0x3c003c00, v10
	s_cbranch_scc1 .LBB2_57
	v_cmp_gt_i32_e32 vcc, 15, v18
	s_and_saveexec_b64 s[4:5], vcc
	s_cbranch_execz .LBB2_52
	v_max_i32_e32 v10, 1, v44
	v_cvt_f32_u32_e32 v10, v10
	v_rcp_iflag_f32_e32 v44, v10
	s_nop 0
	v_pk_mul_f32 v[10:11], v[44:45], s[2:3]
	s_nop 0
	v_mul_f32_e32 v14, 0x4b800000, v10
	v_pk_mul_f32 v[16:17], v[10:11], v[10:11] op_sel:[0,1] op_sel_hi:[1,0]
	s_nop 0
	v_fma_mixlo_f16 v15, v60, v14, v16
	v_pk_fma_f32 v[10:11], v[42:43], v[14:15], v[16:17] op_sel_hi:[1,0,0]
	v_pk_fma_f32 v[12:13], v[36:37], v[14:15], v[16:17] op_sel_hi:[1,0,0]
	v_pk_fma_f32 v[22:23], v[30:31], v[14:15], v[16:17] op_sel_hi:[1,0,0]
	v_cvt_pk_f16_f32 v11, v10, v11
	v_cvt_pk_f16_f32 v12, v12, v13
	v_cvt_pk_f16_f32 v13, v22, v23
	v_pack_b32_f16 v10, v15, v11
	v_alignbit_b32 v11, v12, v11, 16
	v_alignbit_b32 v12, v13, v12, 16
	v_lshrrev_b32_e32 v13, 16, v13
	v_fma_mixhi_f16 v13, v53, v14, v16
	v_add_u32_e32 v14, v18, v77
	v_xor_b32_e32 v15, v14, v0
	v_lshlrev_b32_e32 v15, 4, v15
	v_and_b32_e32 v15, 0xf0, v15
	v_lshl_or_b32 v14, v14, 8, v15
	ds_write_b128 v14, v[10:13]

.LBB2_57:
	s_add_i32 s27, s27, 1
	global_load_dwordx2 v[26:27], v83, s[10:11]
	global_load_dwordx2 v[28:29], v84, s[10:11]
	global_load_dwordx2 v[22:23], v85, s[10:11]
	global_load_dwordx2 v[24:25], v86, s[10:11]
	global_load_dword v56, v87, s[12:13]
	global_load_dword v57, v88, s[12:13]
	global_load_dword v54, v89, s[12:13]
	global_load_dword v55, v90, s[12:13]
	s_cmp_lg_u32 s27, s21
	s_cbranch_scc1 .Lm2_34
	s_cmp_eq_u32 s20, 0
	s_cbranch_scc1 .Lm2_32
	s_add_i32 s27, s20, 1
	s_mov_b32 s20, 2
	s_cmp_eq_u32 s27, 2
	v_mov_b32_e32 v3, v7
	v_mov_b32_e32 v5, v51
	s_mov_b32 s21, s16
	s_cbranch_scc1 .Lm2_33
	s_cmp_eq_u32 s27, 3
	s_cselect_b64 vcc, -1, 0
	s_and_b64 s[20:21], vcc, exec
	v_cndmask_b32_e32 v5, 0, v52, vcc
	s_cselect_b32 s21, s6, 0x7fffffff
	s_mov_b32 s20, s27
	v_mov_b32_e32 v3, v8
	s_branch .Lm2_33
.Lm2_32:
	s_mov_b32 s20, 1
	v_mov_b32_e32 v3, v4
	v_mov_b32_e32 v5, v50
	s_mov_b32 s21, s7

.Lm2_34:
.Lc2_49:
	s_lshl_b32 s28, s27, 2
	v_add_u32_e32 v79, s28, v3
	v_lshl_add_u32 v79, v79, 2, v2
	ds_read_b32 v80, v79 offset:15360
	ds_read_b32 v81, v79 offset:15364
	ds_read_b32 v82, v79 offset:15368
	ds_read_b32 v79, v79 offset:15372
	v_cmp_lt_i32_e32 vcc, s28, v5
	s_or_b32 s29, s28, 1
	s_or_b32 s30, s28, 2
	s_waitcnt lgkmcnt(0)
	v_cndmask_b32_e32 v87, v9, v80, vcc
	v_cmp_lt_i32_e32 vcc, s29, v5
	s_or_b32 s31, s28, 3
	s_nop 0
	v_cndmask_b32_e32 v88, v9, v81, vcc
	v_cmp_lt_i32_e32 vcc, s30, v5
	v_lshl_or_b32 v83, v87, 7, v66
	v_lshlrev_b32_e32 v87, 2, v87
	v_cndmask_b32_e32 v89, v9, v82, vcc
	v_cmp_lt_i32_e32 vcc, s31, v5
	v_lshl_or_b32 v84, v88, 7, v66
	v_lshl_or_b32 v85, v89, 7, v66
	v_cndmask_b32_e32 v90, v9, v79, vcc
	v_lshl_or_b32 v86, v90, 7, v66
	v_lshlrev_b32_e32 v88, 2, v88
	v_lshlrev_b32_e32 v89, 2, v89
	v_lshlrev_b32_e32 v90, 2, v90
	s_waitcnt vmcnt(18)
	v_cvt_pk_f16_f32 v10, v63, v64
	v_perm_b32 v11, v48, v46, s23
	v_dot2c_f32_f16_e32 v60, v11, v10
	v_perm_b32 v11, v48, v46, s24
	v_dot2c_f32_f16_e32 v42, v11, v10
	v_perm_b32 v11, v48, v46, s25
	v_dot2c_f32_f16_e32 v43, v11, v10
	v_perm_b32 v11, v48, v46, s26
	v_dot2c_f32_f16_e32 v36, v11, v10
	v_perm_b32 v11, v49, v47, s23
	v_dot2c_f32_f16_e32 v37, v11, v10
	v_perm_b32 v11, v49, v47, s24
	v_dot2c_f32_f16_e32 v30, v11, v10
	v_perm_b32 v11, v49, v47, s25
	v_dot2c_f32_f16_e32 v31, v11, v10
	v_perm_b32 v11, v49, v47, s26
	v_dot2c_f32_f16_e32 v53, v11, v10
	v_dot2c_f32_f16_e32 v45, 0x3c003c00, v10
	s_waitcnt vmcnt(16)
	v_cvt_pk_f16_f32 v10, v65, v91
	v_perm_b32 v11, v94, v92, s23
	v_dot2c_f32_f16_e32 v60, v11, v10
	v_perm_b32 v11, v94, v92, s24
	v_dot2c_f32_f16_e32 v42, v11, v10
	v_perm_b32 v11, v94, v92, s25
	v_dot2c_f32_f16_e32 v43, v11, v10
	v_perm_b32 v11, v94, v92, s26
	v_dot2c_f32_f16_e32 v36, v11, v10
	v_perm_b32 v11, v95, v93, s23
	v_dot2c_f32_f16_e32 v37, v11, v10
	v_perm_b32 v11, v95, v93, s24
	v_dot2c_f32_f16_e32 v30, v11, v10
	v_perm_b32 v11, v95, v93, s25
	v_dot2c_f32_f16_e32 v31, v11, v10
	v_perm_b32 v11, v95, v93, s26
	s_add_i32 s5, s5, 1
	v_dot2c_f32_f16_e32 v53, v11, v10
	s_cmp_lg_u32 s5, s4
	v_dot2c_f32_f16_e32 v45, 0x3c003c00, v10
	s_cbranch_scc1 .Lc2_57
	v_cmp_gt_i32_e32 vcc, 15, v18
	s_and_saveexec_b64 s[4:5], vcc
	s_cbranch_execz .Lc2_52
	v_max_i32_e32 v10, 1, v44
	v_cvt_f32_u32_e32 v10, v10
	v_rcp_iflag_f32_e32 v44, v10
	s_nop 0
	v_pk_mul_f32 v[10:11], v[44:45], s[2:3]
	s_nop 0
	v_mul_f32_e32 v14, 0x4b800000, v10
	v_pk_mul_f32 v[16:17], v[10:11], v[10:11] op_sel:[0,1] op_sel_hi:[1,0]
	s_nop 0
	v_fma_mixlo_f16 v15, v60, v14, v16
	v_pk_fma_f32 v[10:11], v[42:43], v[14:15], v[16:17] op_sel_hi:[1,0,0]
	v_pk_fma_f32 v[12:13], v[36:37], v[14:15], v[16:17] op_sel_hi:[1,0,0]
	v_pk_fma_f32 v[92:93], v[30:31], v[14:15], v[16:17] op_sel_hi:[1,0,0]
	v_cvt_pk_f16_f32 v11, v10, v11
	v_cvt_pk_f16_f32 v12, v12, v13
	v_cvt_pk_f16_f32 v13, v92, v93
	v_pack_b32_f16 v10, v15, v11
	v_alignbit_b32 v11, v12, v11, 16
	v_alignbit_b32 v12, v13, v12, 16
	v_lshrrev_b32_e32 v13, 16, v13
	v_fma_mixhi_f16 v13, v53, v14, v16
	v_add_u32_e32 v14, v18, v77
	v_xor_b32_e32 v15, v14, v0
	v_lshlrev_b32_e32 v15, 4, v15
	v_and_b32_e32 v15, 0xf0, v15
	v_lshl_or_b32 v14, v14, 8, v15
	ds_write_b128 v14, v[10:13]

.Lc2_57:
	s_add_i32 s27, s27, 1
	global_load_dwordx2 v[46:47], v83, s[10:11]
	global_load_dwordx2 v[48:49], v84, s[10:11]
	global_load_dwordx2 v[92:93], v85, s[10:11]
	global_load_dwordx2 v[94:95], v86, s[10:11]
	global_load_dword v63, v87, s[12:13]
	global_load_dword v64, v88, s[12:13]
	global_load_dword v65, v89, s[12:13]
	global_load_dword v91, v90, s[12:13]
	s_cmp_lg_u32 s27, s21
	s_cbranch_scc1 .LBB2_34
	s_cmp_eq_u32 s20, 0
	s_cbranch_scc1 .LBB2_32
	s_add_i32 s27, s20, 1
	s_mov_b32 s20, 2
	s_cmp_eq_u32 s27, 2
	v_mov_b32_e32 v3, v7
	v_mov_b32_e32 v5, v51
	s_mov_b32 s21, s16
	s_cbranch_scc1 .LBB2_33
	s_cmp_eq_u32 s27, 3
	s_cselect_b64 vcc, -1, 0
	s_and_b64 s[20:21], vcc, exec
	v_cndmask_b32_e32 v5, 0, v52, vcc
	s_cselect_b32 s21, s6, 0x7fffffff
	s_mov_b32 s20, s27
	v_mov_b32_e32 v3, v8
	s_branch .LBB2_33

.LBB2_84:
	s_setprio 2
	v_add_u32_e32 v12, v78, v1
	v_add_u32_e32 v11, 4, v12
	v_add_u32_e32 v13, 8, v12
	v_add_u32_e32 v10, 12, v12
	v_min_i32_e32 v12, 0x1869f, v12
	v_min_i32_e32 v11, 0x1869f, v11
	v_min_i32_e32 v13, 0x1869f, v13
	v_min_i32_e32 v10, 0x1869f, v10
	v_lshl_or_b32 v12, v12, 9, v6
	v_lshl_or_b32 v11, v11, 9, v6
	v_lshl_or_b32 v13, v13, 9, v6
	v_lshl_or_b32 v10, v10, 9, v6
	global_load_dwordx4 v[2:5], v12, s[8:9]
	global_load_dwordx4 v[6:9], v12, s[8:9] offset:16
	global_load_dwordx4 v[14:17], v11, s[8:9]
	global_load_dwordx4 v[78:81], v11, s[8:9] offset:16
	global_load_dwordx4 v[82:85], v13, s[8:9]
	global_load_dwordx4 v[86:89], v13, s[8:9] offset:16
	global_load_dwordx4 v[90:93], v10, s[8:9]
	global_load_dwordx4 v[10:13], v10, s[8:9] offset:16
	s_waitcnt vmcnt(8)
	s_cmp_gt_i32 s17, 3
	s_cbranch_scc1 .LBB2_105
	s_waitcnt vmcnt(18)
	s_mov_b32 s2, 0xc040c00
	v_cvt_pk_f16_f32 v46, v61, v62
	v_perm_b32 v47, v40, v38, s2
	s_mov_b32 s3, 0xc050c01
	v_dot2c_f32_f16_e32 v60, v47, v46
	v_perm_b32 v47, v40, v38, s3
	s_mov_b32 s8, 0xc060c02
	s_mov_b32 s9, 0xc070c03
	v_dot2c_f32_f16_e32 v42, v47, v46
	v_perm_b32 v47, v40, v38, s8
	v_perm_b32 v38, v40, v38, s9
	v_dot2c_f32_f16_e32 v36, v38, v46
	v_perm_b32 v38, v41, v39, s2
	v_dot2c_f32_f16_e32 v37, v38, v46
	v_perm_b32 v38, v41, v39, s3
	v_dot2c_f32_f16_e32 v30, v38, v46
	v_perm_b32 v38, v41, v39, s8
	v_dot2c_f32_f16_e32 v31, v38, v46
	v_perm_b32 v38, v41, v39, s9
	v_dot2c_f32_f16_e32 v53, v38, v46
	s_waitcnt vmcnt(16)
	v_cvt_pk_f16_f32 v38, v58, v59
	v_perm_b32 v39, v34, v32, s2
	v_dot2c_f32_f16_e32 v60, v39, v38
	v_perm_b32 v39, v34, v32, s3
	v_dot2c_f32_f16_e32 v42, v39, v38
	v_perm_b32 v39, v34, v32, s8
	v_perm_b32 v32, v34, v32, s9
	v_dot2c_f32_f16_e32 v36, v32, v38
	v_perm_b32 v32, v35, v33, s2
	v_dot2c_f32_f16_e32 v37, v32, v38
	v_perm_b32 v32, v35, v33, s3
	v_dot2c_f32_f16_e32 v30, v32, v38
	v_perm_b32 v32, v35, v33, s8
	v_dot2c_f32_f16_e32 v43, v47, v46
	v_dot2c_f32_f16_e32 v45, 0x3c003c00, v46
	v_dot2c_f32_f16_e32 v31, v32, v38
	v_perm_b32 v32, v35, v33, s9
	s_add_i32 s5, s5, 1
	v_dot2c_f32_f16_e32 v43, v39, v38
	v_dot2c_f32_f16_e32 v53, v32, v38
	v_dot2c_f32_f16_e32 v45, 0x3c003c00, v38
	s_cmp_lg_u32 s5, s4
	s_mov_b64 s[2:3], -1
	s_cbranch_scc1 .LBB2_102
	v_cmp_gt_i32_e32 vcc, 15, v18
	s_and_saveexec_b64 s[2:3], vcc
	s_cbranch_execz .LBB2_96
	v_max_i32_e32 v32, 1, v44
	v_cvt_f32_u32_e32 v32, v32
	s_mov_b32 s4, 0x3a800000
	s_mov_b32 s5, 0xc3000000
	v_add_u32_e32 v18, v18, v77
	v_rcp_iflag_f32_e32 v44, v32
	s_nop 0
	v_pk_mul_f32 v[32:33], v[44:45], s[4:5]
	s_nop 0
	v_mul_f32_e32 v38, 0x4b800000, v32
	v_pk_mul_f32 v[40:41], v[32:33], v[32:33] op_sel:[0,1] op_sel_hi:[1,0]
	s_nop 0
	v_fma_mixlo_f16 v39, v60, v38, v40
	v_pk_fma_f32 v[32:33], v[42:43], v[38:39], v[40:41] op_sel_hi:[1,0,0]
	v_pk_fma_f32 v[34:35], v[36:37], v[38:39], v[40:41] op_sel_hi:[1,0,0]
	v_pk_fma_f32 v[30:31], v[30:31], v[38:39], v[40:41] op_sel_hi:[1,0,0]
	v_cvt_pk_f16_f32 v33, v32, v33
	v_cvt_pk_f16_f32 v34, v34, v35
	v_cvt_pk_f16_f32 v30, v30, v31
	v_pack_b32_f16 v32, v39, v33
	v_alignbit_b32 v33, v34, v33, 16
	v_alignbit_b32 v34, v30, v34, 16
	v_lshrrev_b32_e32 v35, 16, v30
	v_xor_b32_e32 v30, v18, v0
	v_lshlrev_b32_e32 v30, 4, v30
	v_and_b32_e32 v30, 0xf0, v30
	v_fma_mixhi_f16 v35, v53, v38, v40
	v_lshl_or_b32 v18, v18, 8, v30
	ds_write_b128 v18, v[32:35]

.LBB2_107:
	s_or_b64 exec, exec, s[2:3]
	s_load_dwordx4 s[4:7], s[0:1], 0x38
	s_cmpk_lt_i32 s19, 0x181
	s_cbranch_scc0 .LBB2_62
	s_branch .LBB2_63
	s_nop 0
	s_nop 0
	s_nop 0
	s_nop 0
	s_nop 0
	s_nop 0
	s_nop 0
	s_nop 0
	s_nop 0
	s_nop 0
	s_nop 0
	s_nop 0
	s_nop 0
	s_nop 0
	s_nop 0
	s_nop 0
	s_nop 0
	s_nop 0
	s_nop 0
	s_nop 0
	s_nop 0
	s_nop 0
	s_nop 0
	s_nop 0
	s_nop 0
	s_nop 0
	s_nop 0
	s_nop 0
	s_nop 0
	s_nop 0
	s_nop 0
	s_endpgm
